# grid barrier: non-leader CUs poll the cross-XCD generation word directly instead of waiting for their XCD leader's release hop (12 of 14 sites), on top of v040
# speedup vs baseline: 1.0025x; 1.0013x over previous
.LBB0_429:
	s_or_b64 exec, exec, s[14:15]
	v_cvt_f32_u32_e32 v6, v4
	s_waitcnt vmcnt(0)
	v_readfirstlane_b32 s12, v5
	v_sub_u32_e32 v5, 0, v4
	v_rcp_iflag_f32_e32 v6, v6
	v_add_u32_e32 v7, s12, v1
	v_mul_f32_e32 v6, 0x4f7ffffe, v6
	v_cvt_u32_f32_e32 v6, v6
	v_mul_lo_u32 v1, v5, v6
	v_mul_hi_u32 v1, v6, v1
	v_add_u32_e32 v1, v6, v1
	v_mul_hi_u32 v1, v7, v1
	v_mul_lo_u32 v5, v1, v4
	v_sub_u32_e32 v5, v7, v5
	v_add_u32_e32 v6, 1, v1
	v_cmp_ge_u32_e32 vcc, v5, v4
	s_nop 1
	v_cndmask_b32_e32 v1, v1, v6, vcc
	v_sub_u32_e32 v6, v5, v4
	v_cndmask_b32_e32 v5, v5, v6, vcc
	v_add_u32_e32 v6, 1, v1
	v_cmp_ge_u32_e32 vcc, v5, v4
	v_add_u32_e32 v5, 1, v7
	s_nop 0
	v_cndmask_b32_e32 v1, v1, v6, vcc
	v_mul_lo_u32 v6, v4, v1
	v_add_u32_e32 v4, v6, v4
	v_cmp_ne_u32_e32 vcc, v5, v4
	s_and_saveexec_b64 s[12:13], vcc
	s_xor_b64 s[12:13], exec, s[12:13]
	s_cbranch_execz .LBB0_443
	s_waitcnt lgkmcnt(0)
	s_add_u32 s18, s8, 0x7500
	s_addc_u32 s19, s9, 0
	global_load_dword v2, v3, s[18:19] sc1
	s_nop 0
	s_waitcnt vmcnt(0)
	v_cmp_eq_u32_e32 vcc, v2, v1
	s_and_saveexec_b64 s[14:15], vcc
	s_cbranch_execz .LBB0_442
	s_add_u32 s16, s8, 0x4200
	s_addc_u32 s17, s9, 0
	s_mov_b32 s38, 1
	s_mov_b64 s[22:23], 0
	s_branch .LBB0_433

.LBB0_1446:
	s_or_b64 exec, exec, s[16:17]
	v_cvt_f32_u32_e32 v6, v4
	s_waitcnt vmcnt(0)
	v_readfirstlane_b32 s14, v5
	v_sub_u32_e32 v5, 0, v4
	v_rcp_iflag_f32_e32 v6, v6
	v_add_u32_e32 v7, s14, v1
	v_mul_f32_e32 v6, 0x4f7ffffe, v6
	v_cvt_u32_f32_e32 v6, v6
	v_mul_lo_u32 v1, v5, v6
	v_mul_hi_u32 v1, v6, v1
	v_add_u32_e32 v1, v6, v1
	v_mul_hi_u32 v1, v7, v1
	v_mul_lo_u32 v5, v1, v4
	v_sub_u32_e32 v5, v7, v5
	v_add_u32_e32 v6, 1, v1
	v_cmp_ge_u32_e32 vcc, v5, v4
	s_nop 1
	v_cndmask_b32_e32 v1, v1, v6, vcc
	v_sub_u32_e32 v6, v5, v4
	v_cndmask_b32_e32 v5, v5, v6, vcc
	v_add_u32_e32 v6, 1, v1
	v_cmp_ge_u32_e32 vcc, v5, v4
	v_add_u32_e32 v5, 1, v7
	s_nop 0
	v_cndmask_b32_e32 v1, v1, v6, vcc
	v_mul_lo_u32 v6, v4, v1
	v_add_u32_e32 v4, v6, v4
	v_cmp_ne_u32_e32 vcc, v5, v4
	s_and_saveexec_b64 s[14:15], vcc
	s_xor_b64 s[14:15], exec, s[14:15]
	s_cbranch_execz .LBB0_1460
	s_waitcnt lgkmcnt(0)
	s_add_u32 s22, s8, 0x7500
	s_addc_u32 s23, s9, 0
	global_load_dword v2, v3, s[22:23] sc1
	s_nop 0
	s_waitcnt vmcnt(0)
	v_cmp_eq_u32_e32 vcc, v2, v1
	s_and_saveexec_b64 s[16:17], vcc
	s_cbranch_execz .LBB0_1459
	s_add_u32 s18, s8, 0x4200
	s_addc_u32 s19, s9, 0
	s_mov_b32 s36, 1
	s_mov_b64 s[24:25], 0
	s_branch .LBB0_1450

.LBB0_1532:
	s_or_b64 exec, exec, s[18:19]
	v_cvt_f32_u32_e32 v6, v4
	s_waitcnt vmcnt(0)
	v_readfirstlane_b32 s16, v5
	v_sub_u32_e32 v5, 0, v4
	v_rcp_iflag_f32_e32 v6, v6
	v_add_u32_e32 v7, s16, v1
	v_mul_f32_e32 v6, 0x4f7ffffe, v6
	v_cvt_u32_f32_e32 v6, v6
	v_mul_lo_u32 v1, v5, v6
	v_mul_hi_u32 v1, v6, v1
	v_add_u32_e32 v1, v6, v1
	v_mul_hi_u32 v1, v7, v1
	v_mul_lo_u32 v5, v1, v4
	v_sub_u32_e32 v5, v7, v5
	v_add_u32_e32 v6, 1, v1
	v_cmp_ge_u32_e32 vcc, v5, v4
	s_nop 1
	v_cndmask_b32_e32 v1, v1, v6, vcc
	v_sub_u32_e32 v6, v5, v4
	v_cndmask_b32_e32 v5, v5, v6, vcc
	v_add_u32_e32 v6, 1, v1
	v_cmp_ge_u32_e32 vcc, v5, v4
	v_add_u32_e32 v5, 1, v7
	s_nop 0
	v_cndmask_b32_e32 v1, v1, v6, vcc
	v_mul_lo_u32 v6, v4, v1
	v_add_u32_e32 v4, v6, v4
	v_cmp_ne_u32_e32 vcc, v5, v4
	s_and_saveexec_b64 s[16:17], vcc
	s_xor_b64 s[16:17], exec, s[16:17]
	s_cbranch_execz .LBB0_1546
	s_waitcnt lgkmcnt(0)
	s_add_u32 s24, s10, 0x7500
	s_addc_u32 s25, s11, 0
	global_load_dword v2, v3, s[24:25] sc1
	s_nop 0
	s_waitcnt vmcnt(0)
	v_cmp_eq_u32_e32 vcc, v2, v1
	s_and_saveexec_b64 s[18:19], vcc
	s_cbranch_execz .LBB0_1545
	s_add_u32 s22, s10, 0x4200
	s_addc_u32 s23, s11, 0
	s_mov_b32 s42, 1
	s_mov_b64 s[26:27], 0
	s_branch .LBB0_1536

.LBB0_1801:
	s_or_b64 exec, exec, s[12:13]
	v_cvt_f32_u32_e32 v6, v4
	s_waitcnt vmcnt(0)
	v_readfirstlane_b32 s10, v5
	v_sub_u32_e32 v5, 0, v4
	v_rcp_iflag_f32_e32 v6, v6
	v_add_u32_e32 v7, s10, v1
	v_mul_f32_e32 v6, 0x4f7ffffe, v6
	v_cvt_u32_f32_e32 v6, v6
	v_mul_lo_u32 v1, v5, v6
	v_mul_hi_u32 v1, v6, v1
	v_add_u32_e32 v1, v6, v1
	v_mul_hi_u32 v1, v7, v1
	v_mul_lo_u32 v5, v1, v4
	v_sub_u32_e32 v5, v7, v5
	v_add_u32_e32 v6, 1, v1
	v_cmp_ge_u32_e32 vcc, v5, v4
	s_nop 1
	v_cndmask_b32_e32 v1, v1, v6, vcc
	v_sub_u32_e32 v6, v5, v4
	v_cndmask_b32_e32 v5, v5, v6, vcc
	v_add_u32_e32 v6, 1, v1
	v_cmp_ge_u32_e32 vcc, v5, v4
	v_add_u32_e32 v5, 1, v7
	s_nop 0
	v_cndmask_b32_e32 v1, v1, v6, vcc
	v_mul_lo_u32 v6, v4, v1
	v_add_u32_e32 v4, v6, v4
	v_cmp_ne_u32_e32 vcc, v5, v4
	s_and_saveexec_b64 s[10:11], vcc
	s_xor_b64 s[10:11], exec, s[10:11]
	s_cbranch_execz .LBB0_1815
	s_waitcnt lgkmcnt(0)
	s_add_u32 s16, s6, 0x7500
	s_addc_u32 s17, s7, 0
	global_load_dword v2, v3, s[16:17] sc1
	s_nop 0
	s_waitcnt vmcnt(0)
	v_cmp_eq_u32_e32 vcc, v2, v1
	s_and_saveexec_b64 s[12:13], vcc
	s_cbranch_execz .LBB0_1814
	s_add_u32 s14, s6, 0x4200
	s_addc_u32 s15, s7, 0
	s_mov_b32 s34, 1
	s_mov_b64 s[18:19], 0
	s_branch .LBB0_1805
